# S11: S10 + adj loader issues super-tile 0 loads right after kernargs (row bases computed incrementally), bb0 before S1
# baseline (speedup 1.0000x reference)
.LBB1_65:
	s_andn2_saveexec_b64 s[4:5], s[12:13]
	s_cbranch_execz .LBB1_103
	s_load_dwordx2 s[4:5], s[0:1], 0x0
	s_load_dwordx2 s[6:7], s[0:1], 0x10
	v_mov_b32_e32 v128, v102
	v_readfirstlane_b32 s8, v98
	v_and_b32_e32 v135, 15, v128
	v_lshrrev_b32_e32 v130, 4, v128
	v_lshlrev_b32_e32 v129, 4, v135
	s_add_i32 s8, s8, -8
	s_add_i32 s10, s3, 26
	s_mov_b32 s12, 0x2aaaaaab
	s_add_i32 s11, s3, 0
	v_add_u32_e32 v132, s11, v130
	v_min_u32_e32 v132, s10, v132
	v_mul_hi_u32 v133, v132, s12
	v_lshrrev_b32_e32 v133, 3, v133
	v_mul_u32_u24_e32 v134, 48, v133
	v_sub_u32_e32 v134, v132, v134
	v_mul_u32_u24_e32 v133, 0xc0000, v133
	v_lshl_add_u32 v133, v134, 8, v133
	v_add_u32_e32 v132, v133, v129
	s_mul_i32 s11, s8, 0x30000
	s_waitcnt lgkmcnt(0)
	s_add_u32 s64, s4, s11
	s_addc_u32 s65, s5, 0
	global_load_dwordx4 v[0:3], v132, s[64:65] nt
	s_add_u32 s66, s64, 0x3000
	s_addc_u32 s67, s65, 0
	global_load_dwordx4 v[4:7], v132, s[66:67] nt
	s_add_u32 s68, s66, 0x3000
	s_addc_u32 s69, s67, 0
	global_load_dwordx4 v[8:11], v132, s[68:69] nt
	s_add_u32 s70, s68, 0x3000
	s_addc_u32 s71, s69, 0
	global_load_dwordx4 v[12:15], v132, s[70:71] nt
	s_add_u32 s72, s70, 0x3000
	s_addc_u32 s73, s71, 0
	global_load_dwordx4 v[16:19], v132, s[72:73] nt
	s_add_u32 s74, s72, 0x3000
	s_addc_u32 s75, s73, 0
	global_load_dwordx4 v[20:23], v132, s[74:75] nt
	s_add_u32 s76, s74, 0x3000
	s_addc_u32 s77, s75, 0
	global_load_dwordx4 v[24:27], v132, s[76:77] nt
	s_add_u32 s78, s76, 0x3000
	s_addc_u32 s79, s77, 0
	global_load_dwordx4 v[28:31], v132, s[78:79] nt
	s_add_u32 s80, s78, 0x3000
	s_addc_u32 s81, s79, 0
	global_load_dwordx4 v[32:35], v132, s[80:81] nt
	s_add_u32 s82, s80, 0x3000
	s_addc_u32 s83, s81, 0
	global_load_dwordx4 v[36:39], v132, s[82:83] nt
	s_add_u32 s84, s82, 0x3000
	s_addc_u32 s85, s83, 0
	global_load_dwordx4 v[40:43], v132, s[84:85] nt
	s_add_u32 s86, s84, 0x3000
	s_addc_u32 s87, s85, 0
	global_load_dwordx4 v[44:47], v132, s[86:87] nt
	s_add_u32 s88, s86, 0x3000
	s_addc_u32 s89, s87, 0
	global_load_dwordx4 v[48:51], v132, s[88:89] nt
	s_add_u32 s90, s88, 0x3000
	s_addc_u32 s91, s89, 0
	global_load_dwordx4 v[52:55], v132, s[90:91] nt
	s_add_u32 s92, s90, 0x3000
	s_addc_u32 s93, s91, 0
	global_load_dwordx4 v[56:59], v132, s[92:93] nt
	s_add_u32 s94, s92, 0x3000
	s_addc_u32 s95, s93, 0
	global_load_dwordx4 v[60:63], v132, s[94:95] nt
	v_lshlrev_b32_e32 v138, 4, v128
	s_mul_i32 s9, s28, 48
	s_sub_i32 s9, s3, s9
	s_mul_hi_u32 s11, s28, s12
	s_lshr_b32 s11, s11, 3
	s_mul_i32 s17, s11, 48
	s_sub_i32 s17, s28, s17
	s_mov_b32 s16, s9
	s_mul_i32 s11, s11, 192
	s_lshl_b32 s13, s9, 2
	s_add_i32 s11, s11, s13
	s_lshl_b32 s11, s11, 8
	s_add_u32 s14, s6, s11
	s_addc_u32 s15, s7, 0
	global_load_dwordx4 v[140:143], v138, s[14:15]
	s_add_u32 s14, s14, 0x400
	s_addc_u32 s15, s15, 0
	s_add_i32 s16, s16, 1
	s_cmp_lg_u32 s16, 48
	s_cbranch_scc1 .Lld_bbn0
	s_mov_b32 s16, 0
	s_add_i32 s17, s17, 1
	s_cmp_lg_u32 s17, 48
	s_cbranch_scc1 .Lld_bbw0
	s_mov_b32 s17, 0
	s_branch .Lld_bbn0

.Lld_bbn0:
	s_add_i32 s11, s3, 4
	v_add_u32_e32 v132, s11, v130
	v_min_u32_e32 v132, s10, v132
	v_mul_hi_u32 v133, v132, s12
	v_lshrrev_b32_e32 v133, 3, v133
	v_mul_u32_u24_e32 v134, 48, v133
	v_sub_u32_e32 v134, v132, v134
	v_mul_u32_u24_e32 v133, 0xc0000, v133
	v_lshl_add_u32 v133, v134, 8, v133
	v_add_u32_e32 v132, v133, v129
	global_load_dwordx4 v[64:67], v132, s[64:65] nt
	global_load_dwordx4 v[68:71], v132, s[66:67] nt
	global_load_dwordx4 v[72:75], v132, s[68:69] nt
	global_load_dwordx4 v[76:79], v132, s[70:71] nt
	global_load_dwordx4 v[80:83], v132, s[72:73] nt
	global_load_dwordx4 v[84:87], v132, s[74:75] nt
	global_load_dwordx4 v[88:91], v132, s[76:77] nt
	global_load_dwordx4 v[92:95], v132, s[78:79] nt
	global_load_dwordx4 v[96:99], v132, s[80:81] nt
	global_load_dwordx4 v[100:103], v132, s[82:83] nt
	global_load_dwordx4 v[104:107], v132, s[84:85] nt
	global_load_dwordx4 v[108:111], v132, s[86:87] nt
	global_load_dwordx4 v[112:115], v132, s[88:89] nt
	global_load_dwordx4 v[116:119], v132, s[90:91] nt
	global_load_dwordx4 v[120:123], v132, s[92:93] nt
	global_load_dwordx4 v[124:127], v132, s[94:95] nt
	v_lshrrev_b32_e32 v133, 2, v135
	v_and_b32_e32 v134, 1, v135
	v_bfe_u32 v136, v135, 1, 1
	v_lshl_or_b32 v134, v134, 1, v136
	v_lshlrev_b32_e32 v134, 3, v134
	v_lshl_or_b32 v134, v133, 5, v134
	s_mul_i32 s11, s8, 2304
	s_add_i32 s11, s11, 87040
	s_movk_i32 s13, 9216
	v_mad_u32_u24 v131, v130, s13, v134
	v_add_u32_e32 v131, s11, v131
	global_load_dwordx4 v[144:147], v138, s[14:15]
	s_add_u32 s14, s14, 0x400
	s_addc_u32 s15, s15, 0
	s_add_i32 s16, s16, 1
	s_cmp_lg_u32 s16, 48
	s_cbranch_scc1 .Lld_bbn1
	s_mov_b32 s16, 0
	s_add_i32 s17, s17, 1
	s_cmp_lg_u32 s17, 48
	s_cbranch_scc1 .Lld_bbw1
	s_mov_b32 s17, 0
	s_branch .Lld_bbn1

.Lld_bbn4:
	s_waitcnt vmcnt(36)
	v_med3_i32 v0, v0, 0, 1
	v_med3_i32 v1, v1, 0, 1
	v_med3_i32 v2, v2, 0, 1
	v_med3_i32 v3, v3, 0, 1
	v_lshl_or_b32 v0, v1, 16, v0
	v_lshl_or_b32 v1, v3, 16, v2
	v_mul_u32_u24_e32 v0, 0xffff, v0
	v_mul_u32_u24_e32 v1, 0xffff, v1
	ds_write_b64 v131, v[0:1] offset:0
	s_waitcnt vmcnt(35)
	v_med3_i32 v4, v4, 0, 1
	v_med3_i32 v5, v5, 0, 1
	v_med3_i32 v6, v6, 0, 1
	v_med3_i32 v7, v7, 0, 1
	v_lshl_or_b32 v4, v5, 16, v4
	v_lshl_or_b32 v5, v7, 16, v6
	v_mul_u32_u24_e32 v4, 0xffff, v4
	v_mul_u32_u24_e32 v5, 0xffff, v5
	ds_write_b64 v131, v[4:5] offset:144
	s_waitcnt vmcnt(34)
	v_med3_i32 v8, v8, 0, 1
	v_med3_i32 v9, v9, 0, 1
	v_med3_i32 v10, v10, 0, 1
	v_med3_i32 v11, v11, 0, 1
	v_lshl_or_b32 v8, v9, 16, v8
	v_lshl_or_b32 v9, v11, 16, v10
	v_mul_u32_u24_e32 v8, 0xffff, v8
	v_mul_u32_u24_e32 v9, 0xffff, v9
	ds_write_b64 v131, v[8:9] offset:288
	s_waitcnt vmcnt(33)
	v_med3_i32 v12, v12, 0, 1
	v_med3_i32 v13, v13, 0, 1
	v_med3_i32 v14, v14, 0, 1
	v_med3_i32 v15, v15, 0, 1
	v_lshl_or_b32 v12, v13, 16, v12
	v_lshl_or_b32 v13, v15, 16, v14
	v_mul_u32_u24_e32 v12, 0xffff, v12
	v_mul_u32_u24_e32 v13, 0xffff, v13
	ds_write_b64 v131, v[12:13] offset:432
	s_waitcnt vmcnt(32)
	v_med3_i32 v16, v16, 0, 1
	v_med3_i32 v17, v17, 0, 1
	v_med3_i32 v18, v18, 0, 1
	v_med3_i32 v19, v19, 0, 1
	v_lshl_or_b32 v16, v17, 16, v16
	v_lshl_or_b32 v17, v19, 16, v18
	v_mul_u32_u24_e32 v16, 0xffff, v16
	v_mul_u32_u24_e32 v17, 0xffff, v17
	ds_write_b64 v131, v[16:17] offset:576
	s_waitcnt vmcnt(31)
	v_med3_i32 v20, v20, 0, 1
	v_med3_i32 v21, v21, 0, 1
	v_med3_i32 v22, v22, 0, 1
	v_med3_i32 v23, v23, 0, 1
	v_lshl_or_b32 v20, v21, 16, v20
	v_lshl_or_b32 v21, v23, 16, v22
	v_mul_u32_u24_e32 v20, 0xffff, v20
	v_mul_u32_u24_e32 v21, 0xffff, v21
	ds_write_b64 v131, v[20:21] offset:720
	s_waitcnt vmcnt(30)
	v_med3_i32 v24, v24, 0, 1
	v_med3_i32 v25, v25, 0, 1
	v_med3_i32 v26, v26, 0, 1
	v_med3_i32 v27, v27, 0, 1
	v_lshl_or_b32 v24, v25, 16, v24
	v_lshl_or_b32 v25, v27, 16, v26
	v_mul_u32_u24_e32 v24, 0xffff, v24
	v_mul_u32_u24_e32 v25, 0xffff, v25
	ds_write_b64 v131, v[24:25] offset:864
	s_waitcnt vmcnt(29)
	v_med3_i32 v28, v28, 0, 1
	v_med3_i32 v29, v29, 0, 1
	v_med3_i32 v30, v30, 0, 1
	v_med3_i32 v31, v31, 0, 1
	v_lshl_or_b32 v28, v29, 16, v28
	v_lshl_or_b32 v29, v31, 16, v30
	v_mul_u32_u24_e32 v28, 0xffff, v28
	v_mul_u32_u24_e32 v29, 0xffff, v29
	ds_write_b64 v131, v[28:29] offset:1008
	s_waitcnt vmcnt(28)
	v_med3_i32 v32, v32, 0, 1
	v_med3_i32 v33, v33, 0, 1
	v_med3_i32 v34, v34, 0, 1
	v_med3_i32 v35, v35, 0, 1
	v_lshl_or_b32 v32, v33, 16, v32
	v_lshl_or_b32 v33, v35, 16, v34
	v_mul_u32_u24_e32 v32, 0xffff, v32
	v_mul_u32_u24_e32 v33, 0xffff, v33
	ds_write_b64 v131, v[32:33] offset:1152
	s_waitcnt vmcnt(27)
	v_med3_i32 v36, v36, 0, 1
	v_med3_i32 v37, v37, 0, 1
	v_med3_i32 v38, v38, 0, 1
	v_med3_i32 v39, v39, 0, 1
	v_lshl_or_b32 v36, v37, 16, v36
	v_lshl_or_b32 v37, v39, 16, v38
	v_mul_u32_u24_e32 v36, 0xffff, v36
	v_mul_u32_u24_e32 v37, 0xffff, v37
	ds_write_b64 v131, v[36:37] offset:1296
	s_waitcnt vmcnt(26)
	v_med3_i32 v40, v40, 0, 1
	v_med3_i32 v41, v41, 0, 1
	v_med3_i32 v42, v42, 0, 1
	v_med3_i32 v43, v43, 0, 1
	v_lshl_or_b32 v40, v41, 16, v40
	v_lshl_or_b32 v41, v43, 16, v42
	v_mul_u32_u24_e32 v40, 0xffff, v40
	v_mul_u32_u24_e32 v41, 0xffff, v41
	ds_write_b64 v131, v[40:41] offset:1440
	s_waitcnt vmcnt(25)
	v_med3_i32 v44, v44, 0, 1
	v_med3_i32 v45, v45, 0, 1
	v_med3_i32 v46, v46, 0, 1
	v_med3_i32 v47, v47, 0, 1
	v_lshl_or_b32 v44, v45, 16, v44
	v_lshl_or_b32 v45, v47, 16, v46
	v_mul_u32_u24_e32 v44, 0xffff, v44
	v_mul_u32_u24_e32 v45, 0xffff, v45
	ds_write_b64 v131, v[44:45] offset:1584
	s_waitcnt vmcnt(24)
	v_med3_i32 v48, v48, 0, 1
	v_med3_i32 v49, v49, 0, 1
	v_med3_i32 v50, v50, 0, 1
	v_med3_i32 v51, v51, 0, 1
	v_lshl_or_b32 v48, v49, 16, v48
	v_lshl_or_b32 v49, v51, 16, v50
	v_mul_u32_u24_e32 v48, 0xffff, v48
	v_mul_u32_u24_e32 v49, 0xffff, v49
	ds_write_b64 v131, v[48:49] offset:1728
	s_waitcnt vmcnt(23)
	v_med3_i32 v52, v52, 0, 1
	v_med3_i32 v53, v53, 0, 1
	v_med3_i32 v54, v54, 0, 1
	v_med3_i32 v55, v55, 0, 1
	v_lshl_or_b32 v52, v53, 16, v52
	v_lshl_or_b32 v53, v55, 16, v54
	v_mul_u32_u24_e32 v52, 0xffff, v52
	v_mul_u32_u24_e32 v53, 0xffff, v53
	ds_write_b64 v131, v[52:53] offset:1872
	s_waitcnt vmcnt(22)
	v_med3_i32 v56, v56, 0, 1
	v_med3_i32 v57, v57, 0, 1
	v_med3_i32 v58, v58, 0, 1
	v_med3_i32 v59, v59, 0, 1
	v_lshl_or_b32 v56, v57, 16, v56
	v_lshl_or_b32 v57, v59, 16, v58
	v_mul_u32_u24_e32 v56, 0xffff, v56
	v_mul_u32_u24_e32 v57, 0xffff, v57
	ds_write_b64 v131, v[56:57] offset:2016
	s_waitcnt vmcnt(21)
	v_med3_i32 v60, v60, 0, 1
	v_med3_i32 v61, v61, 0, 1
	v_med3_i32 v62, v62, 0, 1
	v_med3_i32 v63, v63, 0, 1
	v_lshl_or_b32 v60, v61, 16, v60
	v_lshl_or_b32 v61, v63, 16, v62
	v_mul_u32_u24_e32 v60, 0xffff, v60
	v_mul_u32_u24_e32 v61, 0xffff, v61
	ds_write_b64 v131, v[60:61] offset:2160
	s_waitcnt vmcnt(20)
	s_cmp_lg_u32 s8, 0
	s_cbranch_scc1 .Lld_bbs0
	ds_write_b128 v138, v[140:143] offset:18432
.Lld_bbs0:
	s_waitcnt lgkmcnt(0)
	s_add_i32 s11, s3, 8
	v_add_u32_e32 v132, s11, v130
	v_min_u32_e32 v132, s10, v132
	v_mul_hi_u32 v133, v132, s12
	v_lshrrev_b32_e32 v133, 3, v133
	v_mul_u32_u24_e32 v134, 48, v133
	v_sub_u32_e32 v134, v132, v134
	v_mul_u32_u24_e32 v133, 0xc0000, v133
	v_lshl_add_u32 v133, v134, 8, v133
	v_add_u32_e32 v132, v133, v129
	global_load_dwordx4 v[0:3], v132, s[64:65] nt
	global_load_dwordx4 v[4:7], v132, s[66:67] nt
	global_load_dwordx4 v[8:11], v132, s[68:69] nt
	global_load_dwordx4 v[12:15], v132, s[70:71] nt
	global_load_dwordx4 v[16:19], v132, s[72:73] nt
	global_load_dwordx4 v[20:23], v132, s[74:75] nt
	global_load_dwordx4 v[24:27], v132, s[76:77] nt
	global_load_dwordx4 v[28:31], v132, s[78:79] nt
	global_load_dwordx4 v[32:35], v132, s[80:81] nt
	global_load_dwordx4 v[36:39], v132, s[82:83] nt
	global_load_dwordx4 v[40:43], v132, s[84:85] nt
	global_load_dwordx4 v[44:47], v132, s[86:87] nt
	global_load_dwordx4 v[48:51], v132, s[88:89] nt
	global_load_dwordx4 v[52:55], v132, s[90:91] nt
	global_load_dwordx4 v[56:59], v132, s[92:93] nt
	global_load_dwordx4 v[60:63], v132, s[94:95] nt
	s_barrier
	s_waitcnt vmcnt(35)
	v_med3_i32 v64, v64, 0, 1
	v_med3_i32 v65, v65, 0, 1
	v_med3_i32 v66, v66, 0, 1
	v_med3_i32 v67, v67, 0, 1
	v_lshl_or_b32 v64, v65, 16, v64
	v_lshl_or_b32 v65, v67, 16, v66
	v_mul_u32_u24_e32 v64, 0xffff, v64
	v_mul_u32_u24_e32 v65, 0xffff, v65
	ds_write_b64 v131, v[64:65] offset:36864
	s_waitcnt vmcnt(34)
	v_med3_i32 v68, v68, 0, 1
	v_med3_i32 v69, v69, 0, 1
	v_med3_i32 v70, v70, 0, 1
	v_med3_i32 v71, v71, 0, 1
	v_lshl_or_b32 v68, v69, 16, v68
	v_lshl_or_b32 v69, v71, 16, v70
	v_mul_u32_u24_e32 v68, 0xffff, v68
	v_mul_u32_u24_e32 v69, 0xffff, v69
	ds_write_b64 v131, v[68:69] offset:37008
	s_waitcnt vmcnt(33)
	v_med3_i32 v72, v72, 0, 1
	v_med3_i32 v73, v73, 0, 1
	v_med3_i32 v74, v74, 0, 1
	v_med3_i32 v75, v75, 0, 1
	v_lshl_or_b32 v72, v73, 16, v72
	v_lshl_or_b32 v73, v75, 16, v74
	v_mul_u32_u24_e32 v72, 0xffff, v72
	v_mul_u32_u24_e32 v73, 0xffff, v73
	ds_write_b64 v131, v[72:73] offset:37152
	s_waitcnt vmcnt(32)
	v_med3_i32 v76, v76, 0, 1
	v_med3_i32 v77, v77, 0, 1
	v_med3_i32 v78, v78, 0, 1
	v_med3_i32 v79, v79, 0, 1
	v_lshl_or_b32 v76, v77, 16, v76
	v_lshl_or_b32 v77, v79, 16, v78
	v_mul_u32_u24_e32 v76, 0xffff, v76
	v_mul_u32_u24_e32 v77, 0xffff, v77
	ds_write_b64 v131, v[76:77] offset:37296
	s_waitcnt vmcnt(19)
	s_cmp_lg_u32 s8, 0
	s_cbranch_scc1 .Lld_bbs1
	ds_write_b128 v138, v[144:147] offset:19456

.Lld_nf0:
	s_add_i32 s9, s9, 1
	s_cmp_eq_u32 s9, 48
	s_cselect_b32 s9, 0, s9
	s_waitcnt vmcnt(36)
	v_med3_i32 v80, v80, 0, 1
	v_med3_i32 v81, v81, 0, 1
	v_med3_i32 v82, v82, 0, 1
	v_med3_i32 v83, v83, 0, 1
	v_lshl_or_b32 v80, v81, 16, v80
	v_lshl_or_b32 v81, v83, 16, v82
	v_mul_u32_u24_e32 v80, 0xffff, v80
	v_mul_u32_u24_e32 v81, 0xffff, v81
	ds_write_b64 v131, v[80:81] offset:37440
	s_waitcnt vmcnt(35)
	v_med3_i32 v84, v84, 0, 1
	v_med3_i32 v85, v85, 0, 1
	v_med3_i32 v86, v86, 0, 1
	v_med3_i32 v87, v87, 0, 1
	v_lshl_or_b32 v84, v85, 16, v84
	v_lshl_or_b32 v85, v87, 16, v86
	v_mul_u32_u24_e32 v84, 0xffff, v84
	v_mul_u32_u24_e32 v85, 0xffff, v85
	ds_write_b64 v131, v[84:85] offset:37584
	s_waitcnt vmcnt(34)
	v_med3_i32 v88, v88, 0, 1
	v_med3_i32 v89, v89, 0, 1
	v_med3_i32 v90, v90, 0, 1
	v_med3_i32 v91, v91, 0, 1
	v_lshl_or_b32 v88, v89, 16, v88
	v_lshl_or_b32 v89, v91, 16, v90
	v_mul_u32_u24_e32 v88, 0xffff, v88
	v_mul_u32_u24_e32 v89, 0xffff, v89
	ds_write_b64 v131, v[88:89] offset:37728
	s_waitcnt vmcnt(33)
	v_med3_i32 v92, v92, 0, 1
	v_med3_i32 v93, v93, 0, 1
	v_med3_i32 v94, v94, 0, 1
	v_med3_i32 v95, v95, 0, 1
	v_lshl_or_b32 v92, v93, 16, v92
	v_lshl_or_b32 v93, v95, 16, v94
	v_mul_u32_u24_e32 v92, 0xffff, v92
	v_mul_u32_u24_e32 v93, 0xffff, v93
	ds_write_b64 v131, v[92:93] offset:37872
	s_waitcnt vmcnt(23)
	s_cmp_lg_u32 s8, 0
	s_cbranch_scc1 .Lld_bbs2
	ds_write_b128 v138, v[148:151] offset:18432

.Lld_nf1:
	s_add_i32 s9, s9, 1
	s_cmp_eq_u32 s9, 48
	s_cselect_b32 s9, 0, s9
	s_waitcnt vmcnt(37)
	v_med3_i32 v96, v96, 0, 1
	v_med3_i32 v97, v97, 0, 1
	v_med3_i32 v98, v98, 0, 1
	v_med3_i32 v99, v99, 0, 1
	v_lshl_or_b32 v96, v97, 16, v96
	v_lshl_or_b32 v97, v99, 16, v98
	v_mul_u32_u24_e32 v96, 0xffff, v96
	v_mul_u32_u24_e32 v97, 0xffff, v97
	ds_write_b64 v131, v[96:97] offset:38016
	s_waitcnt vmcnt(36)
	v_med3_i32 v100, v100, 0, 1
	v_med3_i32 v101, v101, 0, 1
	v_med3_i32 v102, v102, 0, 1
	v_med3_i32 v103, v103, 0, 1
	v_lshl_or_b32 v100, v101, 16, v100
	v_lshl_or_b32 v101, v103, 16, v102
	v_mul_u32_u24_e32 v100, 0xffff, v100
	v_mul_u32_u24_e32 v101, 0xffff, v101
	ds_write_b64 v131, v[100:101] offset:38160
	s_waitcnt vmcnt(35)
	v_med3_i32 v104, v104, 0, 1
	v_med3_i32 v105, v105, 0, 1
	v_med3_i32 v106, v106, 0, 1
	v_med3_i32 v107, v107, 0, 1
	v_lshl_or_b32 v104, v105, 16, v104
	v_lshl_or_b32 v105, v107, 16, v106
	v_mul_u32_u24_e32 v104, 0xffff, v104
	v_mul_u32_u24_e32 v105, 0xffff, v105
	ds_write_b64 v131, v[104:105] offset:38304
	s_waitcnt vmcnt(34)
	v_med3_i32 v108, v108, 0, 1
	v_med3_i32 v109, v109, 0, 1
	v_med3_i32 v110, v110, 0, 1
	v_med3_i32 v111, v111, 0, 1
	v_lshl_or_b32 v108, v109, 16, v108
	v_lshl_or_b32 v109, v111, 16, v110
	v_mul_u32_u24_e32 v108, 0xffff, v108
	v_mul_u32_u24_e32 v109, 0xffff, v109
	ds_write_b64 v131, v[108:109] offset:38448
	s_waitcnt vmcnt(27)
	s_cmp_lg_u32 s8, 0
	s_cbranch_scc1 .Lld_bbs3
	ds_write_b128 v138, v[152:155] offset:19456

.Lld_nf2:
	s_add_i32 s9, s9, 1
	s_cmp_eq_u32 s9, 48
	s_cselect_b32 s9, 0, s9
	s_waitcnt vmcnt(38)
	v_med3_i32 v112, v112, 0, 1
	v_med3_i32 v113, v113, 0, 1
	v_med3_i32 v114, v114, 0, 1
	v_med3_i32 v115, v115, 0, 1
	v_lshl_or_b32 v112, v113, 16, v112
	v_lshl_or_b32 v113, v115, 16, v114
	v_mul_u32_u24_e32 v112, 0xffff, v112
	v_mul_u32_u24_e32 v113, 0xffff, v113
	ds_write_b64 v131, v[112:113] offset:38592
	s_waitcnt vmcnt(37)
	v_med3_i32 v116, v116, 0, 1
	v_med3_i32 v117, v117, 0, 1
	v_med3_i32 v118, v118, 0, 1
	v_med3_i32 v119, v119, 0, 1
	v_lshl_or_b32 v116, v117, 16, v116
	v_lshl_or_b32 v117, v119, 16, v118
	v_mul_u32_u24_e32 v116, 0xffff, v116
	v_mul_u32_u24_e32 v117, 0xffff, v117
	ds_write_b64 v131, v[116:117] offset:38736
	s_waitcnt vmcnt(36)
	v_med3_i32 v120, v120, 0, 1
	v_med3_i32 v121, v121, 0, 1
	v_med3_i32 v122, v122, 0, 1
	v_med3_i32 v123, v123, 0, 1
	v_lshl_or_b32 v120, v121, 16, v120
	v_lshl_or_b32 v121, v123, 16, v122
	v_mul_u32_u24_e32 v120, 0xffff, v120
	v_mul_u32_u24_e32 v121, 0xffff, v121
	ds_write_b64 v131, v[120:121] offset:38880
	s_waitcnt vmcnt(35)
	v_med3_i32 v124, v124, 0, 1
	v_med3_i32 v125, v125, 0, 1
	v_med3_i32 v126, v126, 0, 1
	v_med3_i32 v127, v127, 0, 1
	v_lshl_or_b32 v124, v125, 16, v124
	v_lshl_or_b32 v125, v127, 16, v126
	v_mul_u32_u24_e32 v124, 0xffff, v124
	v_mul_u32_u24_e32 v125, 0xffff, v125
	ds_write_b64 v131, v[124:125] offset:39024
	s_waitcnt vmcnt(31)
	s_cmp_lg_u32 s8, 0
	s_cbranch_scc1 .Lld_bbs4
	ds_write_b128 v138, v[156:159] offset:18432
